# P1 in-proj epilogue staged through LDS for full-line stores + P9 epilogue pipeline reordered
# speedup vs baseline: 1.0076x; 1.0076x over previous
.LBB0_194:
	s_movk_i32 s66, 0x1ff
	s_movk_i32 s67, 0x4bf
	s_mov_b64 s[68:69], 0x800
	s_lshl_b32 s19, s63, 20
	s_lshl_b32 s22, s64, 9
	s_add_i32 s19, s19, s22
	s_add_u32 s22, s12, s19
	s_addc_u32 s23, s13, 0
	s_nop 15
	s_nop 15
	v_and_b32_e32 v36, 15, v205
	v_lshrrev_b32_e32 v37, 2, v205
	v_and_b32_e32 v37, 16, v37
	v_or_b32_e32 v37, v37, v36
	v_lshrrev_b32_e32 v38, 3, v221
	v_xor_b32_e32 v38, v38, v36
	v_lshlrev_b32_e32 v38, 4, v38
	v_lshl_or_b32 v40, v37, 8, v38
	v_add_u32_e32 v40, 0x21800, v40
	v_lshrrev_b32_e32 v42, 4, v0
	v_and_b32_e32 v43, 15, v0
	v_xor_b32_e32 v44, v43, v42
	v_and_b32_e32 v44, 15, v44
	v_lshlrev_b32_e32 v44, 4, v44
	v_lshl_or_b32 v47, v42, 8, v44
	v_add_u32_e32 v47, 0x21800, v47
	v_and_b32_e32 v45, 15, v42
	v_lshrrev_b32_e32 v46, 4, v42
	v_lshl_or_b32 v45, v46, 6, v45
	v_lshlrev_b32_e32 v45, 12, v45
	v_lshl_or_b32 v45, v43, 4, v45
	v_cvt_pk_bf16_f32 v28, v80, v81
	v_cvt_pk_bf16_f32 v29, v82, v83
	v_cvt_pk_bf16_f32 v30, v88, v89
	v_cvt_pk_bf16_f32 v31, v90, v91
	ds_write_b128 v40, v[28:31]
	v_cvt_pk_bf16_f32 v56, v144, v145
	v_cvt_pk_bf16_f32 v57, v146, v147
	v_cvt_pk_bf16_f32 v58, v154, v155
	v_cvt_pk_bf16_f32 v59, v156, v157
	s_waitcnt lgkmcnt(0)
	s_barrier
	ds_read_b128 v[32:35], v47
	ds_write_b128 v40, v[56:59] offset:12288
	v_cvt_pk_bf16_f32 v28, v96, v97
	v_cvt_pk_bf16_f32 v29, v98, v99
	v_cvt_pk_bf16_f32 v30, v104, v105
	v_cvt_pk_bf16_f32 v31, v106, v107
	s_waitcnt lgkmcnt(1)
	global_store_dwordx4 v45, v[32:35], s[22:23]
	s_add_u32 s22, s22, 0x100
	s_addc_u32 s23, s23, 0
	s_waitcnt lgkmcnt(0)
	s_barrier
	ds_read_b128 v[48:51], v47 offset:12288
	ds_write_b128 v40, v[28:31]
	v_cvt_pk_bf16_f32 v56, v158, v159
	v_cvt_pk_bf16_f32 v57, v160, v161
	v_cvt_pk_bf16_f32 v58, v162, v163
	v_cvt_pk_bf16_f32 v59, v164, v165
	s_waitcnt lgkmcnt(1)
	global_store_dwordx4 v45, v[48:51], s[22:23]
	s_add_u32 s22, s22, 0xff00
	s_addc_u32 s23, s23, 0
	s_waitcnt lgkmcnt(0)
	s_barrier
	ds_read_b128 v[32:35], v47
	ds_write_b128 v40, v[56:59] offset:12288
	v_cvt_pk_bf16_f32 v28, v112, v113
	v_cvt_pk_bf16_f32 v29, v114, v115
	v_cvt_pk_bf16_f32 v30, v120, v121
	v_cvt_pk_bf16_f32 v31, v122, v123
	s_waitcnt lgkmcnt(1)
	global_store_dwordx4 v45, v[32:35], s[22:23]
	s_add_u32 s22, s22, 0x100
	s_addc_u32 s23, s23, 0
	s_waitcnt lgkmcnt(0)
	s_barrier
	ds_read_b128 v[48:51], v47 offset:12288
	ds_write_b128 v40, v[28:31]
	v_cvt_pk_bf16_f32 v56, v166, v167
	v_cvt_pk_bf16_f32 v57, v168, v169
	v_cvt_pk_bf16_f32 v58, v170, v171
	v_cvt_pk_bf16_f32 v59, v172, v173
	s_waitcnt lgkmcnt(1)
	global_store_dwordx4 v45, v[48:51], s[22:23]
	s_add_u32 s22, s22, 0xff00
	s_addc_u32 s23, s23, 0
	s_waitcnt lgkmcnt(0)
	s_barrier
	ds_read_b128 v[32:35], v47
	ds_write_b128 v40, v[56:59] offset:12288
	v_cvt_pk_bf16_f32 v28, v128, v129
	v_cvt_pk_bf16_f32 v29, v130, v131
	v_cvt_pk_bf16_f32 v30, v132, v133
	v_cvt_pk_bf16_f32 v31, v134, v135
	s_waitcnt lgkmcnt(1)
	global_store_dwordx4 v45, v[32:35], s[22:23]
	s_add_u32 s22, s22, 0x100
	s_addc_u32 s23, s23, 0
	s_waitcnt lgkmcnt(0)
	s_barrier
	ds_read_b128 v[48:51], v47 offset:12288
	ds_write_b128 v40, v[28:31]
	v_cvt_pk_bf16_f32 v56, v174, v175
	v_cvt_pk_bf16_f32 v57, v176, v177
	v_cvt_pk_bf16_f32 v58, v182, v183
	v_cvt_pk_bf16_f32 v59, v184, v185
	s_waitcnt lgkmcnt(1)
	global_store_dwordx4 v45, v[48:51], s[22:23]
	s_add_u32 s22, s22, 0xff00
	s_addc_u32 s23, s23, 0
	s_waitcnt lgkmcnt(0)
	s_barrier
	ds_read_b128 v[32:35], v47
	ds_write_b128 v40, v[56:59] offset:12288
	v_cvt_pk_bf16_f32 v28, v68, v69
	v_cvt_pk_bf16_f32 v29, v70, v71
	v_cvt_pk_bf16_f32 v30, v72, v73
	v_cvt_pk_bf16_f32 v31, v74, v75
	s_waitcnt lgkmcnt(1)
	global_store_dwordx4 v45, v[32:35], s[22:23]
	s_add_u32 s22, s22, 0x100
	s_addc_u32 s23, s23, 0
	s_waitcnt lgkmcnt(0)
	s_barrier
	ds_read_b128 v[48:51], v47 offset:12288
	ds_write_b128 v40, v[28:31]
	v_cvt_pk_bf16_f32 v56, v124, v125
	v_cvt_pk_bf16_f32 v57, v126, v127
	v_cvt_pk_bf16_f32 v58, v136, v137
	v_cvt_pk_bf16_f32 v59, v138, v139
	s_waitcnt lgkmcnt(1)
	global_store_dwordx4 v45, v[48:51], s[22:23]
	s_add_u32 s22, s22, 0x4ff00
	s_addc_u32 s23, s23, 0
	s_waitcnt lgkmcnt(0)
	s_barrier
	ds_read_b128 v[32:35], v47
	ds_write_b128 v40, v[56:59] offset:12288
	v_cvt_pk_bf16_f32 v28, v76, v77
	v_cvt_pk_bf16_f32 v29, v78, v79
	v_cvt_pk_bf16_f32 v30, v84, v85
	v_cvt_pk_bf16_f32 v31, v86, v87
	s_waitcnt lgkmcnt(1)
	global_store_dwordx4 v45, v[32:35], s[22:23]
	s_add_u32 s22, s22, 0x100
	s_addc_u32 s23, s23, 0
	s_waitcnt lgkmcnt(0)
	s_barrier
	ds_read_b128 v[48:51], v47 offset:12288
	ds_write_b128 v40, v[28:31]
	v_cvt_pk_bf16_f32 v56, v140, v141
	v_cvt_pk_bf16_f32 v57, v142, v143
	v_cvt_pk_bf16_f32 v58, v150, v151
	v_cvt_pk_bf16_f32 v59, v152, v153
	s_waitcnt lgkmcnt(1)
	global_store_dwordx4 v45, v[48:51], s[22:23]
	s_add_u32 s22, s22, 0xff00
	s_addc_u32 s23, s23, 0
	s_waitcnt lgkmcnt(0)
	s_barrier
	ds_read_b128 v[32:35], v47
	ds_write_b128 v40, v[56:59] offset:12288
	v_cvt_pk_bf16_f32 v28, v92, v93
	v_cvt_pk_bf16_f32 v29, v94, v95
	v_cvt_pk_bf16_f32 v30, v100, v101
	v_cvt_pk_bf16_f32 v31, v102, v103
	s_waitcnt lgkmcnt(1)
	global_store_dwordx4 v45, v[32:35], s[22:23]
	s_add_u32 s22, s22, 0x100
	s_addc_u32 s23, s23, 0
	s_waitcnt lgkmcnt(0)
	s_barrier
	ds_read_b128 v[48:51], v47 offset:12288
	ds_write_b128 v40, v[28:31]
	v_cvt_pk_bf16_f32 v56, v178, v179
	v_cvt_pk_bf16_f32 v57, v180, v181
	v_cvt_pk_bf16_f32 v58, v186, v187
	v_cvt_pk_bf16_f32 v59, v188, v189
	s_waitcnt lgkmcnt(1)
	global_store_dwordx4 v45, v[48:51], s[22:23]
	s_add_u32 s22, s22, 0xff00
	s_addc_u32 s23, s23, 0
	s_waitcnt lgkmcnt(0)
	s_barrier
	ds_read_b128 v[32:35], v47
	ds_write_b128 v40, v[56:59] offset:12288
	v_cvt_pk_bf16_f32 v28, v108, v109
	v_cvt_pk_bf16_f32 v29, v110, v111
	v_cvt_pk_bf16_f32 v30, v116, v117
	v_cvt_pk_bf16_f32 v31, v118, v119
	s_waitcnt lgkmcnt(1)
	global_store_dwordx4 v45, v[32:35], s[22:23]
	s_add_u32 s22, s22, 0x100
	s_addc_u32 s23, s23, 0
	s_waitcnt lgkmcnt(0)
	s_barrier
	ds_read_b128 v[48:51], v47 offset:12288
	ds_write_b128 v40, v[28:31]
	v_cvt_pk_bf16_f32 v56, v190, v191
	v_cvt_pk_bf16_f32 v57, v192, v193
	v_cvt_pk_bf16_f32 v58, v194, v195
	v_cvt_pk_bf16_f32 v59, v196, v197
	s_waitcnt lgkmcnt(1)
	global_store_dwordx4 v45, v[48:51], s[22:23]
	s_add_u32 s22, s22, 0xff00
	s_addc_u32 s23, s23, 0
	s_waitcnt lgkmcnt(0)
	s_barrier
	ds_read_b128 v[32:35], v47
	ds_write_b128 v40, v[56:59] offset:12288
	s_waitcnt lgkmcnt(1)
	global_store_dwordx4 v45, v[32:35], s[22:23]
	s_add_u32 s22, s22, 0x100
	s_addc_u32 s23, s23, 0
	s_waitcnt lgkmcnt(0)
	s_barrier
	ds_read_b128 v[48:51], v47 offset:12288
	s_waitcnt lgkmcnt(0)
	global_store_dwordx4 v45, v[48:51], s[22:23]
	s_mov_b64 s[22:23], -1
	s_and_b64 vcc, exec, s[40:41]
	s_cbranch_vccnz .LBB0_173
	s_andn2_b64 vcc, exec, s[10:11]
	s_cbranch_vccnz .LBB0_172
	s_barrier
	s_branch .LBB0_172

.LBB0_996:
	s_lshl_b32 s21, s23, 10
	s_and_b32 s21, s21, 0x400
	s_nop 15
	s_nop 15
	v_add_u32_e32 v2, s21, v205
	ds_read_b128 v[12:15], v2
	ds_read_b128 v[16:19], v2 offset:16
	ds_read_b128 v[4:7], v2 offset:512
	ds_read_b128 v[8:11], v2 offset:528
	v_and_b32_e32 v36, 15, v221
	v_lshrrev_b32_e32 v37, 2, v221
	v_and_b32_e32 v37, 16, v37
	v_or_b32_e32 v37, v37, v36
	v_lshrrev_b32_e32 v38, 4, v209
	v_xor_b32_e32 v38, v38, v36
	v_lshlrev_b32_e32 v38, 4, v38
	v_and_b32_e32 v39, 8, v209
	v_or_b32_e32 v38, v38, v39
	v_lshl_or_b32 v40, v37, 8, v38
	v_add_u32_e32 v40, 0x21800, v40
	v_xor_b32_e32 v41, 0x80, v40
	v_lshrrev_b32_e32 v42, 4, v0
	v_and_b32_e32 v43, 15, v0
	v_xor_b32_e32 v44, v43, v42
	v_and_b32_e32 v44, 15, v44
	v_lshlrev_b32_e32 v44, 4, v44
	v_lshl_or_b32 v47, v42, 8, v44
	v_add_u32_e32 v47, 0x21800, v47
	v_and_b32_e32 v45, 15, v42
	v_lshrrev_b32_e32 v46, 4, v42
	v_lshl_or_b32 v45, v46, 6, v45
	v_lshlrev_b32_e32 v45, 10, v45
	v_lshl_or_b32 v45, v43, 4, v45
	s_lshl_b32 s3, s22, 8
	s_and_b32 s3, s3, 0x300
	s_lshl_b32 s40, s69, 18
	s_add_i32 s3, s3, s40
	s_add_u32 s40, s14, s3
	s_addc_u32 s41, s15, 0
	s_waitcnt lgkmcnt(0)
	v_pk_add_f32 v[20:21], v[80:81], v[12:13]
	v_pk_add_f32 v[22:23], v[88:89], v[16:17]
	v_mov_b32_e32 v28, v3
	v_mov_b32_e32 v29, v3
	v_pk_add_f32 v[24:25], v[82:83], v[14:15]
	v_pk_add_f32 v[26:27], v[90:91], v[18:19]
	v_cvt_pk_fp8_f32 v28, v20, v21
	v_cvt_pk_fp8_f32 v29, v22, v23
	v_cvt_pk_fp8_f32 v28, v24, v25 op_sel:[0,0,1]
	v_cvt_pk_fp8_f32 v29, v26, v27 op_sel:[0,0,1]
	v_pk_add_f32 v[20:21], v[144:145], v[4:5]
	v_pk_add_f32 v[22:23], v[154:155], v[8:9]
	v_mov_b32_e32 v30, v3
	v_mov_b32_e32 v31, v3
	v_pk_add_f32 v[24:25], v[146:147], v[6:7]
	v_pk_add_f32 v[26:27], v[156:157], v[10:11]
	v_cvt_pk_fp8_f32 v30, v20, v21
	v_cvt_pk_fp8_f32 v31, v22, v23
	v_cvt_pk_fp8_f32 v30, v24, v25 op_sel:[0,0,1]
	v_cvt_pk_fp8_f32 v31, v26, v27 op_sel:[0,0,1]
	ds_write_b64 v40, v[28:29]
	ds_write_b64 v41, v[30:31]
	v_pk_add_f32 v[20:21], v[96:97], v[12:13]
	v_pk_add_f32 v[22:23], v[104:105], v[16:17]
	v_mov_b32_e32 v56, v3
	v_mov_b32_e32 v57, v3
	v_pk_add_f32 v[24:25], v[98:99], v[14:15]
	v_pk_add_f32 v[26:27], v[106:107], v[18:19]
	v_cvt_pk_fp8_f32 v56, v20, v21
	v_cvt_pk_fp8_f32 v57, v22, v23
	v_cvt_pk_fp8_f32 v56, v24, v25 op_sel:[0,0,1]
	v_cvt_pk_fp8_f32 v57, v26, v27 op_sel:[0,0,1]
	v_pk_add_f32 v[20:21], v[158:159], v[4:5]
	v_pk_add_f32 v[22:23], v[162:163], v[8:9]
	v_mov_b32_e32 v58, v3
	v_mov_b32_e32 v59, v3
	v_pk_add_f32 v[24:25], v[160:161], v[6:7]
	v_pk_add_f32 v[26:27], v[164:165], v[10:11]
	v_cvt_pk_fp8_f32 v58, v20, v21
	v_cvt_pk_fp8_f32 v59, v22, v23
	v_cvt_pk_fp8_f32 v58, v24, v25 op_sel:[0,0,1]
	v_cvt_pk_fp8_f32 v59, v26, v27 op_sel:[0,0,1]
	s_waitcnt lgkmcnt(0)
	s_barrier
	ds_read_b128 v[32:35], v47
	ds_write_b64 v40, v[56:57] offset:12288
	ds_write_b64 v41, v[58:59] offset:12288
	v_pk_add_f32 v[20:21], v[112:113], v[12:13]
	v_pk_add_f32 v[22:23], v[120:121], v[16:17]
	v_mov_b32_e32 v28, v3
	v_mov_b32_e32 v29, v3
	v_pk_add_f32 v[24:25], v[114:115], v[14:15]
	v_pk_add_f32 v[26:27], v[122:123], v[18:19]
	v_cvt_pk_fp8_f32 v28, v20, v21
	v_cvt_pk_fp8_f32 v29, v22, v23
	v_cvt_pk_fp8_f32 v28, v24, v25 op_sel:[0,0,1]
	v_cvt_pk_fp8_f32 v29, v26, v27 op_sel:[0,0,1]
	v_pk_add_f32 v[20:21], v[166:167], v[4:5]
	v_pk_add_f32 v[22:23], v[170:171], v[8:9]
	v_mov_b32_e32 v30, v3
	v_mov_b32_e32 v31, v3
	v_pk_add_f32 v[24:25], v[168:169], v[6:7]
	v_pk_add_f32 v[26:27], v[172:173], v[10:11]
	v_cvt_pk_fp8_f32 v30, v20, v21
	v_cvt_pk_fp8_f32 v31, v22, v23
	v_cvt_pk_fp8_f32 v30, v24, v25 op_sel:[0,0,1]
	v_cvt_pk_fp8_f32 v31, v26, v27 op_sel:[0,0,1]
	s_waitcnt lgkmcnt(2)
	global_store_dwordx4 v45, v[32:35], s[40:41]
	s_add_u32 s40, s40, 0x4000
	s_addc_u32 s41, s41, 0
	s_waitcnt lgkmcnt(0)
	s_barrier
	ds_read_b128 v[48:51], v47 offset:12288
	ds_write_b64 v40, v[28:29]
	ds_write_b64 v41, v[30:31]
	v_pk_add_f32 v[20:21], v[128:129], v[12:13]
	v_pk_add_f32 v[22:23], v[132:133], v[16:17]
	v_mov_b32_e32 v56, v3
	v_mov_b32_e32 v57, v3
	v_pk_add_f32 v[24:25], v[130:131], v[14:15]
	v_pk_add_f32 v[26:27], v[134:135], v[18:19]
	v_cvt_pk_fp8_f32 v56, v20, v21
	v_cvt_pk_fp8_f32 v57, v22, v23
	v_cvt_pk_fp8_f32 v56, v24, v25 op_sel:[0,0,1]
	v_cvt_pk_fp8_f32 v57, v26, v27 op_sel:[0,0,1]
	v_pk_add_f32 v[20:21], v[174:175], v[4:5]
	v_pk_add_f32 v[22:23], v[182:183], v[8:9]
	v_mov_b32_e32 v58, v3
	v_mov_b32_e32 v59, v3
	v_pk_add_f32 v[24:25], v[176:177], v[6:7]
	v_pk_add_f32 v[26:27], v[184:185], v[10:11]
	v_cvt_pk_fp8_f32 v58, v20, v21
	v_cvt_pk_fp8_f32 v59, v22, v23
	v_cvt_pk_fp8_f32 v58, v24, v25 op_sel:[0,0,1]
	v_cvt_pk_fp8_f32 v59, v26, v27 op_sel:[0,0,1]
	s_waitcnt lgkmcnt(2)
	global_store_dwordx4 v45, v[48:51], s[40:41]
	s_add_u32 s40, s40, 0x4000
	s_addc_u32 s41, s41, 0
	s_waitcnt lgkmcnt(0)
	s_barrier
	ds_read_b128 v[32:35], v47
	ds_write_b64 v40, v[56:57] offset:12288
	ds_write_b64 v41, v[58:59] offset:12288
	v_pk_add_f32 v[20:21], v[68:69], v[12:13]
	v_pk_add_f32 v[22:23], v[72:73], v[16:17]
	v_mov_b32_e32 v28, v3
	v_mov_b32_e32 v29, v3
	v_pk_add_f32 v[24:25], v[70:71], v[14:15]
	v_pk_add_f32 v[26:27], v[74:75], v[18:19]
	v_cvt_pk_fp8_f32 v28, v20, v21
	v_cvt_pk_fp8_f32 v29, v22, v23
	v_cvt_pk_fp8_f32 v28, v24, v25 op_sel:[0,0,1]
	v_cvt_pk_fp8_f32 v29, v26, v27 op_sel:[0,0,1]
	v_pk_add_f32 v[20:21], v[124:125], v[4:5]
	v_pk_add_f32 v[22:23], v[136:137], v[8:9]
	v_mov_b32_e32 v30, v3
	v_mov_b32_e32 v31, v3
	v_pk_add_f32 v[24:25], v[126:127], v[6:7]
	v_pk_add_f32 v[26:27], v[138:139], v[10:11]
	v_cvt_pk_fp8_f32 v30, v20, v21
	v_cvt_pk_fp8_f32 v31, v22, v23
	v_cvt_pk_fp8_f32 v30, v24, v25 op_sel:[0,0,1]
	v_cvt_pk_fp8_f32 v31, v26, v27 op_sel:[0,0,1]
	s_waitcnt lgkmcnt(2)
	global_store_dwordx4 v45, v[32:35], s[40:41]
	s_add_u32 s40, s40, 0x4000
	s_addc_u32 s41, s41, 0
	s_waitcnt lgkmcnt(0)
	s_barrier
	ds_read_b128 v[48:51], v47 offset:12288
	ds_write_b64 v40, v[28:29]
	ds_write_b64 v41, v[30:31]
	v_pk_add_f32 v[20:21], v[76:77], v[12:13]
	v_pk_add_f32 v[22:23], v[84:85], v[16:17]
	v_mov_b32_e32 v56, v3
	v_mov_b32_e32 v57, v3
	v_pk_add_f32 v[24:25], v[78:79], v[14:15]
	v_pk_add_f32 v[26:27], v[86:87], v[18:19]
	v_cvt_pk_fp8_f32 v56, v20, v21
	v_cvt_pk_fp8_f32 v57, v22, v23
	v_cvt_pk_fp8_f32 v56, v24, v25 op_sel:[0,0,1]
	v_cvt_pk_fp8_f32 v57, v26, v27 op_sel:[0,0,1]
	v_pk_add_f32 v[20:21], v[140:141], v[4:5]
	v_pk_add_f32 v[22:23], v[150:151], v[8:9]
	v_mov_b32_e32 v58, v3
	v_mov_b32_e32 v59, v3
	v_pk_add_f32 v[24:25], v[142:143], v[6:7]
	v_pk_add_f32 v[26:27], v[152:153], v[10:11]
	v_cvt_pk_fp8_f32 v58, v20, v21
	v_cvt_pk_fp8_f32 v59, v22, v23
	v_cvt_pk_fp8_f32 v58, v24, v25 op_sel:[0,0,1]
	v_cvt_pk_fp8_f32 v59, v26, v27 op_sel:[0,0,1]
	s_waitcnt lgkmcnt(2)
	global_store_dwordx4 v45, v[48:51], s[40:41]
	s_add_u32 s40, s40, 0x14000
	s_addc_u32 s41, s41, 0
	s_waitcnt lgkmcnt(0)
	s_barrier
	ds_read_b128 v[32:35], v47
	ds_write_b64 v40, v[56:57] offset:12288
	ds_write_b64 v41, v[58:59] offset:12288
	v_pk_add_f32 v[20:21], v[92:93], v[12:13]
	v_pk_add_f32 v[22:23], v[100:101], v[16:17]
	v_mov_b32_e32 v28, v3
	v_mov_b32_e32 v29, v3
	v_pk_add_f32 v[24:25], v[94:95], v[14:15]
	v_pk_add_f32 v[26:27], v[102:103], v[18:19]
	v_cvt_pk_fp8_f32 v28, v20, v21
	v_cvt_pk_fp8_f32 v29, v22, v23
	v_cvt_pk_fp8_f32 v28, v24, v25 op_sel:[0,0,1]
	v_cvt_pk_fp8_f32 v29, v26, v27 op_sel:[0,0,1]
	v_pk_add_f32 v[20:21], v[178:179], v[4:5]
	v_pk_add_f32 v[22:23], v[186:187], v[8:9]
	v_mov_b32_e32 v30, v3
	v_mov_b32_e32 v31, v3
	v_pk_add_f32 v[24:25], v[180:181], v[6:7]
	v_pk_add_f32 v[26:27], v[188:189], v[10:11]
	v_cvt_pk_fp8_f32 v30, v20, v21
	v_cvt_pk_fp8_f32 v31, v22, v23
	v_cvt_pk_fp8_f32 v30, v24, v25 op_sel:[0,0,1]
	v_cvt_pk_fp8_f32 v31, v26, v27 op_sel:[0,0,1]
	s_waitcnt lgkmcnt(2)
	global_store_dwordx4 v45, v[32:35], s[40:41]
	s_add_u32 s40, s40, 0x4000
	s_addc_u32 s41, s41, 0
	s_waitcnt lgkmcnt(0)
	s_barrier
	ds_read_b128 v[48:51], v47 offset:12288
	ds_write_b64 v40, v[28:29]
	ds_write_b64 v41, v[30:31]
	v_pk_add_f32 v[20:21], v[108:109], v[12:13]
	v_pk_add_f32 v[22:23], v[116:117], v[16:17]
	v_mov_b32_e32 v56, v3
	v_mov_b32_e32 v57, v3
	v_pk_add_f32 v[24:25], v[110:111], v[14:15]
	v_pk_add_f32 v[26:27], v[118:119], v[18:19]
	v_cvt_pk_fp8_f32 v56, v20, v21
	v_cvt_pk_fp8_f32 v57, v22, v23
	v_cvt_pk_fp8_f32 v56, v24, v25 op_sel:[0,0,1]
	v_cvt_pk_fp8_f32 v57, v26, v27 op_sel:[0,0,1]
	v_pk_add_f32 v[20:21], v[190:191], v[4:5]
	v_pk_add_f32 v[22:23], v[194:195], v[8:9]
	v_mov_b32_e32 v58, v3
	v_mov_b32_e32 v59, v3
	v_pk_add_f32 v[24:25], v[192:193], v[6:7]
	v_pk_add_f32 v[26:27], v[196:197], v[10:11]
	v_cvt_pk_fp8_f32 v58, v20, v21
	v_cvt_pk_fp8_f32 v59, v22, v23
	v_cvt_pk_fp8_f32 v58, v24, v25 op_sel:[0,0,1]
	v_cvt_pk_fp8_f32 v59, v26, v27 op_sel:[0,0,1]
	s_waitcnt lgkmcnt(2)
	global_store_dwordx4 v45, v[48:51], s[40:41]
	s_add_u32 s40, s40, 0x4000
	s_addc_u32 s41, s41, 0
	s_waitcnt lgkmcnt(0)
	s_barrier
	ds_read_b128 v[32:35], v47
	ds_write_b64 v40, v[56:57] offset:12288
	ds_write_b64 v41, v[58:59] offset:12288
	s_waitcnt lgkmcnt(2)
	global_store_dwordx4 v45, v[32:35], s[40:41]
	s_add_u32 s40, s40, 0x4000
	s_addc_u32 s41, s41, 0
	s_waitcnt lgkmcnt(0)
	s_barrier
	ds_read_b128 v[48:51], v47 offset:12288
	s_waitcnt lgkmcnt(0)
	global_store_dwordx4 v45, v[48:51], s[40:41]
	s_cmp_eq_u32 s23, s66
	s_mov_b64 s[22:23], -1
	s_cbranch_scc1 .LBB0_979
	s_andn2_b64 vcc, exec, s[8:9]
	s_cbranch_vccnz .LBB0_999
	s_ashr_i32 s22, s20, 2
	s_ashr_i32 s23, s22, 31
	s_lshl_b64 s[22:23], s[22:23], 12
	s_add_u32 s3, s52, s22
	s_addc_u32 s21, s53, s23
	s_lshl_b32 s22, s20, 10
	s_and_b32 s22, s22, 0xc00
	s_add_u32 s22, s3, s22
	s_addc_u32 s23, s21, 0
	s_lshl_b32 s3, s68, 10
	s_and_b32 s3, s3, 0x400
	s_add_i32 s3, s3, 0
	s_add_i32 m0, s3, 0x24000
	s_nop 0
	global_load_lds_dwordx4 v223, s[22:23]
